# EpiIn rotary (q_dil/k_dil) epilogue rewritten by hand: packed-f32 rotation/scale, fma form, no pair-shuffle moves (852 vs 1445 instr), on top of prologue + chain DMA reorder
# speedup vs baseline: 1.0084x; 1.0084x over previous
; #define GAS __attribute__((address_space(1)))
; DI unsigned pk4_fp8(float a, float b, float c_, float d) { int w = 0; w = __builtin_amdgcn_cvt_pk_fp8_f32(clamp8(a), clamp8(b), w, false); w = __builtin_amdgcn_cvt_pk_fp8_f32(clamp8(c_), clamp8(d), w, true); return (unsigned)w; }
; DI int in_tile(int pt) { return (pt >= 5 && pt <= 7) ? pt + 30 : ((pt >= 35 && pt <= 37) ? pt - 30 : pt); }
;     DI void operator()(const f32x4 (&acc)[2][2][4][2], const Unit& u, int wr, int wc, int fr, int fq) const {
;     ...
;         const int row0 = u.pm * 256 + wr * 64 + fr; const int pn = in_tile(u.pn);
;         if (pn >= 12 && pn < 24) {
;             bf16_t* base = pn < 18 ? qd : kd; const int tq = pn < 18 ? pn - 12 : pn - 18; const float sc = pn < 18 ? 0.125f * LOG2E * W8_INV : W8_INV;
;             float fre[8];
; #pragma unroll
;             for (int i = 0; i < 8; ++i) fre[i] = __builtin_amdgcn_exp2f(-(float)(8 * fq + i) * (13.287712379549449f / 32.0f)) * 0.15915494309189535f;
;             int posv[8];
; #pragma unroll
;             for (int q = 0; q < 8; ++q) posv[q] = ((const GAS int*)pos)[row0 + (q >> 2) * 128 + (q & 3) * 16];
; #pragma unroll
;             for (int ai = 0; ai < 2; ++ai) {
; #pragma unroll
;                 for (int m = 0; m < 4; ++m) {
;                     const int r = row0 + ai * 128 + m * 16; const float p = (float)posv[ai * 4 + m];
;                     unsigned char* rowp = (unsigned char*)base + dil_row(4 * tq + wc, r) + 8 * fq;
;                     u32x2 w1, w2;
; #pragma unroll
;                     for (int n = 0; n < 2; ++n) { f32x4 o1, o2;
; #pragma unroll
;                         for (int j = 0; j < 4; ++j) {
;                             float a = p * fre[n * 4 + j]; a = a - __builtin_floorf(a);
;                             const float sn = __builtin_amdgcn_sinf(a), cs = __builtin_amdgcn_cosf(a);
;                             const float x1 = acc[ai][0][m][n][j], x2 = acc[ai][1][m][n][j];
;                             o1[j] = (x1 * cs - x2 * sn) * sc; o2[j] = (x2 * cs + x1 * sn) * sc;
;                         }
;                         w1[n] = pk4_fp8(o1[0], o1[1], o1[2], o1[3]); w2[n] = pk4_fp8(o2[0], o2[1], o2[2], o2[3]); }
.LBB0_300:
	v_ashrrev_i32_e32 v11, 31, v10
	s_cmp_lt_u32 s43, 18
	v_lshl_add_u64 v[8:9], v[10:11], 2, s[74:75]
	s_cselect_b64 vcc, -1, 0
	global_load_dword v22, v[8:9], off
	global_load_dword v23, v[8:9], off offset:64
	global_load_dword v24, v[8:9], off offset:128
	global_load_dword v25, v[8:9], off offset:192
	global_load_dword v26, v[8:9], off offset:512
	global_load_dword v27, v[8:9], off offset:576
	global_load_dword v28, v[8:9], off offset:640
	global_load_dword v29, v[8:9], off offset:704
	v_mov_b32_e32 v6, 0x3c800000
	v_mov_b32_e32 v7, 0x3b38aa3b
	v_cndmask_b32_e32 v12, v6, v7, vcc
	v_lshlrev_b32_e32 v6, 3, v18
	s_and_b64 s[4:5], vcc, exec
	s_mov_b32 s4, 0x2cbc0000
	s_cselect_b32 s4, s4, 0x32bc0000
	s_add_u32 s16, s58, s4
	s_addc_u32 s17, s59, 0
	s_and_b64 s[4:5], vcc, exec
	s_cselect_b32 s4, -12, 0xffffffee
	s_add_i32 s5, s4, s43
	s_and_b32 s4, s5, -2
	s_lshl_b32 s5, s5, 17
	s_lshl_b32 s30, -1, s4
	s_or_b32 s31, s5, s97
	s_lshr_b32 s5, 0x1000, s4
	v_bfe_i32 v8, v18, 0, 1
	v_and_b32_e32 v8, 24, v8
	v_mov_b32_e32 v9, v4
	v_mov_b32_e32 v13, v12
	v_cvt_f32_i32_e32 v30, v6
	v_or_b32_e32 v31, 1, v6
	v_cvt_f32_i32_e32 v31, v31
	v_or_b32_e32 v32, 2, v6
	v_cvt_f32_i32_e32 v32, v32
	v_or_b32_e32 v33, 3, v6
	v_cvt_f32_i32_e32 v33, v33
	v_or_b32_e32 v34, 4, v6
	v_cvt_f32_i32_e32 v34, v34
	v_or_b32_e32 v35, 5, v6
	v_cvt_f32_i32_e32 v35, v35
	v_or_b32_e32 v36, 6, v6
	v_cvt_f32_i32_e32 v36, v36
	v_or_b32_e32 v37, 7, v6
	v_cvt_f32_i32_e32 v37, v37
	v_mul_f32_e32 v30, 0xbed49a78, v30
	v_mul_f32_e32 v31, 0xbed49a78, v31
	v_mul_f32_e32 v32, 0xbed49a78, v32
	v_mul_f32_e32 v33, 0xbed49a78, v33
	v_mul_f32_e32 v34, 0xbed49a78, v34
	v_mul_f32_e32 v35, 0xbed49a78, v35
	v_mul_f32_e32 v36, 0xbed49a78, v36
	v_mul_f32_e32 v37, 0xbed49a78, v37
	v_exp_f32_e32 v30, v30
	v_exp_f32_e32 v31, v31
	v_exp_f32_e32 v32, v32
	v_exp_f32_e32 v33, v33
	v_exp_f32_e32 v34, v34
	v_exp_f32_e32 v35, v35
	v_exp_f32_e32 v36, v36
	v_exp_f32_e32 v37, v37
	v_mul_f32_e32 v14, 0x3e22f983, v30
	v_mul_f32_e32 v15, 0x3e22f983, v31
	v_mul_f32_e32 v16, 0x3e22f983, v32
	v_mul_f32_e32 v17, 0x3e22f983, v33
	v_mul_f32_e32 v18, 0x3e22f983, v34
	v_mul_f32_e32 v19, 0x3e22f983, v35
	v_mul_f32_e32 v20, 0x3e22f983, v36
	v_mul_f32_e32 v21, 0x3e22f983, v37
	v_ashrrev_i32_e32 v7, 31, v6
	v_lshl_add_u64 v[6:7], s[16:17], 0, v[6:7]
	v_lshl_add_u64 v[6:7], v[6:7], 0, v[8:9]
	s_waitcnt vmcnt(0)
	v_mov_b32_e32 v11, v10
	v_and_b32_e32 v9, 0xfff, v11
	v_lshrrev_b32_e32 v9, s4, v9
	v_and_b32_e32 v8, 0xfffff000, v11
	v_bitop3_b32 v11, v11, s30, v208 bitop3:0x20
	v_mad_u32_u24 v180, v11, s5, v9
	v_mov_b32_e32 v181, v4
	v_add_u32_e32 v8, s31, v8
	v_ashrrev_i32_e32 v9, 31, v8
	v_lshl_add_u64 v[8:9], v[180:181], 0, v[8:9]
	v_lshlrev_b64 v[8:9], 6, v[8:9]
	v_lshl_add_u64 v[8:9], v[6:7], 0, v[8:9]
	v_cvt_f32_i32_e32 v22, v22
	v_pk_mul_f32 v[34:35], v[14:15], v[22:23] op_sel_hi:[1,0]
	v_pk_mul_f32 v[36:37], v[16:17], v[22:23] op_sel_hi:[1,0]
	v_floor_f32_e32 v30, v34
	v_floor_f32_e32 v31, v35
	v_floor_f32_e32 v32, v36
	v_floor_f32_e32 v33, v37
	v_pk_fma_f32 v[34:35], v[14:15], v[22:23], v[30:31] op_sel_hi:[1,0,1] neg_lo:[0,0,1] neg_hi:[0,0,1]
	v_pk_fma_f32 v[36:37], v[16:17], v[22:23], v[32:33] op_sel_hi:[1,0,1] neg_lo:[0,0,1] neg_hi:[0,0,1]
	v_sin_f32_e32 v30, v34
	v_sin_f32_e32 v31, v35
	v_sin_f32_e32 v32, v36
	v_sin_f32_e32 v33, v37
	v_cos_f32_e32 v34, v34
	v_cos_f32_e32 v35, v35
	v_cos_f32_e32 v36, v36
	v_cos_f32_e32 v37, v37
	v_pk_mul_f32 v[180:181], v[158:159], v[34:35]
	v_pk_mul_f32 v[182:183], v[160:161], v[36:37]
	v_pk_fma_f32 v[180:181], v[162:163], v[30:31], v[180:181] neg_lo:[1,0,0] neg_hi:[1,0,0]
	v_pk_fma_f32 v[182:183], v[164:165], v[32:33], v[182:183] neg_lo:[1,0,0] neg_hi:[1,0,0]
	v_pk_mul_f32 v[162:163], v[162:163], v[34:35]
	v_pk_mul_f32 v[164:165], v[164:165], v[36:37]
	v_pk_fma_f32 v[162:163], v[158:159], v[30:31], v[162:163]
	v_pk_fma_f32 v[164:165], v[160:161], v[32:33], v[164:165]
	v_pk_mul_f32 v[158:159], v[180:181], v[12:13]
	v_pk_mul_f32 v[160:161], v[182:183], v[12:13]
	v_pk_mul_f32 v[162:163], v[162:163], v[12:13]
	v_pk_mul_f32 v[164:165], v[164:165], v[12:13]
	v_med3_f32 v158, v158, s35, v225
	v_med3_f32 v159, v159, s35, v225
	v_med3_f32 v160, v160, s35, v225
	v_med3_f32 v161, v161, s35, v225
	v_med3_f32 v162, v162, s35, v225
	v_med3_f32 v163, v163, s35, v225
	v_med3_f32 v164, v164, s35, v225
	v_med3_f32 v165, v165, s35, v225
	v_pk_mul_f32 v[34:35], v[18:19], v[22:23] op_sel_hi:[1,0]
	v_pk_mul_f32 v[36:37], v[20:21], v[22:23] op_sel_hi:[1,0]
	v_floor_f32_e32 v30, v34
	v_floor_f32_e32 v31, v35
	v_floor_f32_e32 v32, v36
	v_floor_f32_e32 v33, v37
	v_pk_fma_f32 v[34:35], v[18:19], v[22:23], v[30:31] op_sel_hi:[1,0,1] neg_lo:[0,0,1] neg_hi:[0,0,1]
	v_pk_fma_f32 v[36:37], v[20:21], v[22:23], v[32:33] op_sel_hi:[1,0,1] neg_lo:[0,0,1] neg_hi:[0,0,1]
	v_sin_f32_e32 v30, v34
	v_sin_f32_e32 v31, v35
	v_sin_f32_e32 v32, v36
	v_sin_f32_e32 v33, v37
	v_cos_f32_e32 v34, v34
	v_cos_f32_e32 v35, v35
	v_cos_f32_e32 v36, v36
	v_cos_f32_e32 v37, v37
	v_pk_mul_f32 v[180:181], v[150:151], v[34:35]
	v_pk_mul_f32 v[182:183], v[152:153], v[36:37]
	v_pk_fma_f32 v[180:181], v[154:155], v[30:31], v[180:181] neg_lo:[1,0,0] neg_hi:[1,0,0]
	v_pk_fma_f32 v[182:183], v[156:157], v[32:33], v[182:183] neg_lo:[1,0,0] neg_hi:[1,0,0]
	v_pk_mul_f32 v[154:155], v[154:155], v[34:35]
	v_pk_mul_f32 v[156:157], v[156:157], v[36:37]
	v_pk_fma_f32 v[154:155], v[150:151], v[30:31], v[154:155]
	v_pk_fma_f32 v[156:157], v[152:153], v[32:33], v[156:157]
	v_pk_mul_f32 v[150:151], v[180:181], v[12:13]
	v_pk_mul_f32 v[152:153], v[182:183], v[12:13]
	v_pk_mul_f32 v[154:155], v[154:155], v[12:13]
	v_pk_mul_f32 v[156:157], v[156:157], v[12:13]
; DI unsigned pk4_fp8(float a, float b, float c_, float d) { int w = 0; w = __builtin_amdgcn_cvt_pk_fp8_f32(clamp8(a), clamp8(b), w, false); w = __builtin_amdgcn_cvt_pk_fp8_f32(clamp8(c_), clamp8(d), w, true); return (unsigned)w; }
;     DI void operator()(const f32x4 (&acc)[2][2][4][2], const Unit& u, int wr, int wc, int fr, int fq) const {
;     ...
;             for (int ai = 0; ai < 2; ++ai) {
; #pragma unroll
;                 for (int m = 0; m < 4; ++m) {
;                     const int r = row0 + ai * 128 + m * 16; const float p = (float)posv[ai * 4 + m];
;                     unsigned char* rowp = (unsigned char*)base + dil_row(4 * tq + wc, r) + 8 * fq;
;                     u32x2 w1, w2;
; #pragma unroll
;                     for (int n = 0; n < 2; ++n) { f32x4 o1, o2;
; #pragma unroll
;                         for (int j = 0; j < 4; ++j) {
;                             float a = p * fre[n * 4 + j]; a = a - __builtin_floorf(a);
;                             const float sn = __builtin_amdgcn_sinf(a), cs = __builtin_amdgcn_cosf(a);
;                             const float x1 = acc[ai][0][m][n][j], x2 = acc[ai][1][m][n][j];
;                             o1[j] = (x1 * cs - x2 * sn) * sc; o2[j] = (x2 * cs + x1 * sn) * sc;
;                         }
;                         w1[n] = pk4_fp8(o1[0], o1[1], o1[2], o1[3]); w2[n] = pk4_fp8(o2[0], o2[1], o2[2], o2[3]); }
;                     st_pair16(rowp, 32, w1, w2, fq);
;                     asm volatile("" ::: "memory");
	v_med3_f32 v150, v150, s35, v225
	v_med3_f32 v151, v151, s35, v225
	v_med3_f32 v152, v152, s35, v225
	v_med3_f32 v153, v153, s35, v225
	v_med3_f32 v154, v154, s35, v225
	v_med3_f32 v155, v155, s35, v225
	v_med3_f32 v156, v156, s35, v225
	v_med3_f32 v157, v157, s35, v225
	v_cvt_pk_fp8_f32 v158, v158, v159
	v_cvt_pk_fp8_f32 v159, v150, v151
	v_cvt_pk_fp8_f32 v158, v160, v161 op_sel:[0,0,1]
	v_cvt_pk_fp8_f32 v159, v152, v153 op_sel:[0,0,1]
	v_cvt_pk_fp8_f32 v160, v162, v163
	v_cvt_pk_fp8_f32 v161, v154, v155
	v_cvt_pk_fp8_f32 v160, v164, v165 op_sel:[0,0,1]
	v_cvt_pk_fp8_f32 v161, v156, v157 op_sel:[0,0,1]
	s_nop 1
	v_permlane16_swap_b32_e32 v158, v160
	v_permlane16_swap_b32_e32 v159, v161
	global_store_dwordx4 v[8:9], v[158:161], off
	v_add_u32_e32 v11, 0x10, v10
	v_and_b32_e32 v9, 0xfff, v11
	v_lshrrev_b32_e32 v9, s4, v9
	v_and_b32_e32 v8, 0xfffff000, v11
	v_bitop3_b32 v11, v11, s30, v208 bitop3:0x20
	v_mad_u32_u24 v180, v11, s5, v9
	v_mov_b32_e32 v181, v4
	v_add_u32_e32 v8, s31, v8
	v_ashrrev_i32_e32 v9, 31, v8
	v_lshl_add_u64 v[8:9], v[180:181], 0, v[8:9]
	v_lshlrev_b64 v[8:9], 6, v[8:9]
	v_lshl_add_u64 v[8:9], v[6:7], 0, v[8:9]
	v_cvt_f32_i32_e32 v23, v23
	v_pk_mul_f32 v[34:35], v[14:15], v[22:23] op_sel:[0,1] op_sel_hi:[1,1]
	v_pk_mul_f32 v[36:37], v[16:17], v[22:23] op_sel:[0,1] op_sel_hi:[1,1]
	v_floor_f32_e32 v30, v34
	v_floor_f32_e32 v31, v35
	v_floor_f32_e32 v32, v36
	v_floor_f32_e32 v33, v37
	v_pk_fma_f32 v[34:35], v[14:15], v[22:23], v[30:31] op_sel:[0,1,0] op_sel_hi:[1,1,1] neg_lo:[0,0,1] neg_hi:[0,0,1]
	v_pk_fma_f32 v[36:37], v[16:17], v[22:23], v[32:33] op_sel:[0,1,0] op_sel_hi:[1,1,1] neg_lo:[0,0,1] neg_hi:[0,0,1]
	v_sin_f32_e32 v30, v34
	v_sin_f32_e32 v31, v35
	v_sin_f32_e32 v32, v36
	v_sin_f32_e32 v33, v37
	v_cos_f32_e32 v34, v34
	v_cos_f32_e32 v35, v35
	v_cos_f32_e32 v36, v36
	v_cos_f32_e32 v37, v37
	v_pk_mul_f32 v[180:181], v[142:143], v[34:35]
	v_pk_mul_f32 v[182:183], v[144:145], v[36:37]
	v_pk_fma_f32 v[180:181], v[146:147], v[30:31], v[180:181] neg_lo:[1,0,0] neg_hi:[1,0,0]
	v_pk_fma_f32 v[182:183], v[148:149], v[32:33], v[182:183] neg_lo:[1,0,0] neg_hi:[1,0,0]
	v_pk_mul_f32 v[146:147], v[146:147], v[34:35]
	v_pk_mul_f32 v[148:149], v[148:149], v[36:37]
	v_pk_fma_f32 v[146:147], v[142:143], v[30:31], v[146:147]
	v_pk_fma_f32 v[148:149], v[144:145], v[32:33], v[148:149]
	v_pk_mul_f32 v[142:143], v[180:181], v[12:13]
	v_pk_mul_f32 v[144:145], v[182:183], v[12:13]
	v_pk_mul_f32 v[146:147], v[146:147], v[12:13]
	v_pk_mul_f32 v[148:149], v[148:149], v[12:13]
	v_med3_f32 v142, v142, s35, v225
	v_med3_f32 v143, v143, s35, v225
	v_med3_f32 v144, v144, s35, v225
	v_med3_f32 v145, v145, s35, v225
	v_med3_f32 v146, v146, s35, v225
	v_med3_f32 v147, v147, s35, v225
	v_med3_f32 v148, v148, s35, v225
	v_med3_f32 v149, v149, s35, v225
	v_pk_mul_f32 v[34:35], v[18:19], v[22:23] op_sel:[0,1] op_sel_hi:[1,1]
	v_pk_mul_f32 v[36:37], v[20:21], v[22:23] op_sel:[0,1] op_sel_hi:[1,1]
	v_floor_f32_e32 v30, v34
	v_floor_f32_e32 v31, v35
	v_floor_f32_e32 v32, v36
	v_floor_f32_e32 v33, v37
	v_pk_fma_f32 v[34:35], v[18:19], v[22:23], v[30:31] op_sel:[0,1,0] op_sel_hi:[1,1,1] neg_lo:[0,0,1] neg_hi:[0,0,1]
	v_pk_fma_f32 v[36:37], v[20:21], v[22:23], v[32:33] op_sel:[0,1,0] op_sel_hi:[1,1,1] neg_lo:[0,0,1] neg_hi:[0,0,1]
	v_sin_f32_e32 v30, v34
	v_sin_f32_e32 v31, v35
	v_sin_f32_e32 v32, v36
	v_sin_f32_e32 v33, v37
	v_cos_f32_e32 v34, v34
	v_cos_f32_e32 v35, v35
	v_cos_f32_e32 v36, v36
	v_cos_f32_e32 v37, v37
	v_pk_mul_f32 v[180:181], v[134:135], v[34:35]
	v_pk_mul_f32 v[182:183], v[136:137], v[36:37]
	v_pk_fma_f32 v[180:181], v[138:139], v[30:31], v[180:181] neg_lo:[1,0,0] neg_hi:[1,0,0]
	v_pk_fma_f32 v[182:183], v[140:141], v[32:33], v[182:183] neg_lo:[1,0,0] neg_hi:[1,0,0]
	v_pk_mul_f32 v[138:139], v[138:139], v[34:35]
	v_pk_mul_f32 v[140:141], v[140:141], v[36:37]
	v_pk_fma_f32 v[138:139], v[134:135], v[30:31], v[138:139]
	v_pk_fma_f32 v[140:141], v[136:137], v[32:33], v[140:141]
	v_pk_mul_f32 v[134:135], v[180:181], v[12:13]
	v_pk_mul_f32 v[136:137], v[182:183], v[12:13]
	v_pk_mul_f32 v[138:139], v[138:139], v[12:13]
	v_pk_mul_f32 v[140:141], v[140:141], v[12:13]
	v_med3_f32 v134, v134, s35, v225
	v_med3_f32 v135, v135, s35, v225
	v_med3_f32 v136, v136, s35, v225
	v_med3_f32 v137, v137, s35, v225
	v_med3_f32 v138, v138, s35, v225
	v_med3_f32 v139, v139, s35, v225
	v_med3_f32 v140, v140, s35, v225
	v_med3_f32 v141, v141, s35, v225
	v_cvt_pk_fp8_f32 v142, v142, v143
	v_cvt_pk_fp8_f32 v143, v134, v135
	v_cvt_pk_fp8_f32 v142, v144, v145 op_sel:[0,0,1]
	v_cvt_pk_fp8_f32 v143, v136, v137 op_sel:[0,0,1]
	v_cvt_pk_fp8_f32 v144, v146, v147
	v_cvt_pk_fp8_f32 v145, v138, v139
	v_cvt_pk_fp8_f32 v144, v148, v149 op_sel:[0,0,1]
	v_cvt_pk_fp8_f32 v145, v140, v141 op_sel:[0,0,1]
	s_nop 1
	v_permlane16_swap_b32_e32 v142, v144
	v_permlane16_swap_b32_e32 v143, v145
	global_store_dwordx4 v[8:9], v[142:145], off
	v_add_u32_e32 v11, 0x20, v10
	v_and_b32_e32 v9, 0xfff, v11
	v_lshrrev_b32_e32 v9, s4, v9
	v_and_b32_e32 v8, 0xfffff000, v11
	v_bitop3_b32 v11, v11, s30, v208 bitop3:0x20
	v_mad_u32_u24 v180, v11, s5, v9
	v_mov_b32_e32 v181, v4
	v_add_u32_e32 v8, s31, v8
	v_ashrrev_i32_e32 v9, 31, v8
	v_lshl_add_u64 v[8:9], v[180:181], 0, v[8:9]
	v_lshlrev_b64 v[8:9], 6, v[8:9]
	v_lshl_add_u64 v[8:9], v[6:7], 0, v[8:9]
	v_cvt_f32_i32_e32 v24, v24
	v_pk_mul_f32 v[34:35], v[14:15], v[24:25] op_sel_hi:[1,0]
	v_pk_mul_f32 v[36:37], v[16:17], v[24:25] op_sel_hi:[1,0]
	v_floor_f32_e32 v30, v34
	v_floor_f32_e32 v31, v35
	v_floor_f32_e32 v32, v36
	v_floor_f32_e32 v33, v37
	v_pk_fma_f32 v[34:35], v[14:15], v[24:25], v[30:31] op_sel_hi:[1,0,1] neg_lo:[0,0,1] neg_hi:[0,0,1]
; DI unsigned pk4_fp8(float a, float b, float c_, float d) { int w = 0; w = __builtin_amdgcn_cvt_pk_fp8_f32(clamp8(a), clamp8(b), w, false); w = __builtin_amdgcn_cvt_pk_fp8_f32(clamp8(c_), clamp8(d), w, true); return (unsigned)w; }
;     DI void operator()(const f32x4 (&acc)[2][2][4][2], const Unit& u, int wr, int wc, int fr, int fq) const {
;     ...
;             for (int ai = 0; ai < 2; ++ai) {
; #pragma unroll
;                 for (int m = 0; m < 4; ++m) {
;                     const int r = row0 + ai * 128 + m * 16; const float p = (float)posv[ai * 4 + m];
;                     unsigned char* rowp = (unsigned char*)base + dil_row(4 * tq + wc, r) + 8 * fq;
;                     u32x2 w1, w2;
; #pragma unroll
;                     for (int n = 0; n < 2; ++n) { f32x4 o1, o2;
; #pragma unroll
;                         for (int j = 0; j < 4; ++j) {
;                             float a = p * fre[n * 4 + j]; a = a - __builtin_floorf(a);
;                             const float sn = __builtin_amdgcn_sinf(a), cs = __builtin_amdgcn_cosf(a);
;                             const float x1 = acc[ai][0][m][n][j], x2 = acc[ai][1][m][n][j];
;                             o1[j] = (x1 * cs - x2 * sn) * sc; o2[j] = (x2 * cs + x1 * sn) * sc;
;                         }
;                         w1[n] = pk4_fp8(o1[0], o1[1], o1[2], o1[3]); w2[n] = pk4_fp8(o2[0], o2[1], o2[2], o2[3]); }
;                     st_pair16(rowp, 32, w1, w2, fq);
;                     asm volatile("" ::: "memory");
	v_pk_fma_f32 v[36:37], v[16:17], v[24:25], v[32:33] op_sel_hi:[1,0,1] neg_lo:[0,0,1] neg_hi:[0,0,1]
	v_sin_f32_e32 v30, v34
	v_sin_f32_e32 v31, v35
	v_sin_f32_e32 v32, v36
	v_sin_f32_e32 v33, v37
	v_cos_f32_e32 v34, v34
	v_cos_f32_e32 v35, v35
	v_cos_f32_e32 v36, v36
	v_cos_f32_e32 v37, v37
	v_pk_mul_f32 v[180:181], v[126:127], v[34:35]
	v_pk_mul_f32 v[182:183], v[128:129], v[36:37]
	v_pk_fma_f32 v[180:181], v[130:131], v[30:31], v[180:181] neg_lo:[1,0,0] neg_hi:[1,0,0]
	v_pk_fma_f32 v[182:183], v[132:133], v[32:33], v[182:183] neg_lo:[1,0,0] neg_hi:[1,0,0]
	v_pk_mul_f32 v[130:131], v[130:131], v[34:35]
	v_pk_mul_f32 v[132:133], v[132:133], v[36:37]
	v_pk_fma_f32 v[130:131], v[126:127], v[30:31], v[130:131]
	v_pk_fma_f32 v[132:133], v[128:129], v[32:33], v[132:133]
	v_pk_mul_f32 v[126:127], v[180:181], v[12:13]
	v_pk_mul_f32 v[128:129], v[182:183], v[12:13]
	v_pk_mul_f32 v[130:131], v[130:131], v[12:13]
	v_pk_mul_f32 v[132:133], v[132:133], v[12:13]
	v_med3_f32 v126, v126, s35, v225
	v_med3_f32 v127, v127, s35, v225
	v_med3_f32 v128, v128, s35, v225
	v_med3_f32 v129, v129, s35, v225
	v_med3_f32 v130, v130, s35, v225
	v_med3_f32 v131, v131, s35, v225
	v_med3_f32 v132, v132, s35, v225
	v_med3_f32 v133, v133, s35, v225
	v_pk_mul_f32 v[34:35], v[18:19], v[24:25] op_sel_hi:[1,0]
	v_pk_mul_f32 v[36:37], v[20:21], v[24:25] op_sel_hi:[1,0]
	v_floor_f32_e32 v30, v34
	v_floor_f32_e32 v31, v35
	v_floor_f32_e32 v32, v36
	v_floor_f32_e32 v33, v37
	v_pk_fma_f32 v[34:35], v[18:19], v[24:25], v[30:31] op_sel_hi:[1,0,1] neg_lo:[0,0,1] neg_hi:[0,0,1]
	v_pk_fma_f32 v[36:37], v[20:21], v[24:25], v[32:33] op_sel_hi:[1,0,1] neg_lo:[0,0,1] neg_hi:[0,0,1]
	v_sin_f32_e32 v30, v34
	v_sin_f32_e32 v31, v35
	v_sin_f32_e32 v32, v36
	v_sin_f32_e32 v33, v37
	v_cos_f32_e32 v34, v34
	v_cos_f32_e32 v35, v35
	v_cos_f32_e32 v36, v36
	v_cos_f32_e32 v37, v37
	v_pk_mul_f32 v[180:181], v[118:119], v[34:35]
	v_pk_mul_f32 v[182:183], v[120:121], v[36:37]
	v_pk_fma_f32 v[180:181], v[122:123], v[30:31], v[180:181] neg_lo:[1,0,0] neg_hi:[1,0,0]
	v_pk_fma_f32 v[182:183], v[124:125], v[32:33], v[182:183] neg_lo:[1,0,0] neg_hi:[1,0,0]
	v_pk_mul_f32 v[122:123], v[122:123], v[34:35]
	v_pk_mul_f32 v[124:125], v[124:125], v[36:37]
	v_pk_fma_f32 v[122:123], v[118:119], v[30:31], v[122:123]
	v_pk_fma_f32 v[124:125], v[120:121], v[32:33], v[124:125]
	v_pk_mul_f32 v[118:119], v[180:181], v[12:13]
	v_pk_mul_f32 v[120:121], v[182:183], v[12:13]
	v_pk_mul_f32 v[122:123], v[122:123], v[12:13]
	v_pk_mul_f32 v[124:125], v[124:125], v[12:13]
	v_med3_f32 v118, v118, s35, v225
	v_med3_f32 v119, v119, s35, v225
	v_med3_f32 v120, v120, s35, v225
	v_med3_f32 v121, v121, s35, v225
	v_med3_f32 v122, v122, s35, v225
	v_med3_f32 v123, v123, s35, v225
	v_med3_f32 v124, v124, s35, v225
	v_med3_f32 v125, v125, s35, v225
	v_cvt_pk_fp8_f32 v126, v126, v127
	v_cvt_pk_fp8_f32 v127, v118, v119
	v_cvt_pk_fp8_f32 v126, v128, v129 op_sel:[0,0,1]
	v_cvt_pk_fp8_f32 v127, v120, v121 op_sel:[0,0,1]
	v_cvt_pk_fp8_f32 v128, v130, v131
	v_cvt_pk_fp8_f32 v129, v122, v123
	v_cvt_pk_fp8_f32 v128, v132, v133 op_sel:[0,0,1]
	v_cvt_pk_fp8_f32 v129, v124, v125 op_sel:[0,0,1]
	s_nop 1
	v_permlane16_swap_b32_e32 v126, v128
	v_permlane16_swap_b32_e32 v127, v129
	global_store_dwordx4 v[8:9], v[126:129], off
	v_add_u32_e32 v11, 0x30, v10
	v_and_b32_e32 v9, 0xfff, v11
	v_lshrrev_b32_e32 v9, s4, v9
	v_and_b32_e32 v8, 0xfffff000, v11
	v_bitop3_b32 v11, v11, s30, v208 bitop3:0x20
	v_mad_u32_u24 v180, v11, s5, v9
	v_mov_b32_e32 v181, v4
	v_add_u32_e32 v8, s31, v8
	v_ashrrev_i32_e32 v9, 31, v8
	v_lshl_add_u64 v[8:9], v[180:181], 0, v[8:9]
	v_lshlrev_b64 v[8:9], 6, v[8:9]
	v_lshl_add_u64 v[8:9], v[6:7], 0, v[8:9]
	v_cvt_f32_i32_e32 v25, v25
	v_pk_mul_f32 v[34:35], v[14:15], v[24:25] op_sel:[0,1] op_sel_hi:[1,1]
	v_pk_mul_f32 v[36:37], v[16:17], v[24:25] op_sel:[0,1] op_sel_hi:[1,1]
	v_floor_f32_e32 v30, v34
	v_floor_f32_e32 v31, v35
	v_floor_f32_e32 v32, v36
	v_floor_f32_e32 v33, v37
	v_pk_fma_f32 v[34:35], v[14:15], v[24:25], v[30:31] op_sel:[0,1,0] op_sel_hi:[1,1,1] neg_lo:[0,0,1] neg_hi:[0,0,1]
	v_pk_fma_f32 v[36:37], v[16:17], v[24:25], v[32:33] op_sel:[0,1,0] op_sel_hi:[1,1,1] neg_lo:[0,0,1] neg_hi:[0,0,1]
	v_sin_f32_e32 v30, v34
	v_sin_f32_e32 v31, v35
	v_sin_f32_e32 v32, v36
	v_sin_f32_e32 v33, v37
	v_cos_f32_e32 v34, v34
	v_cos_f32_e32 v35, v35
	v_cos_f32_e32 v36, v36
	v_cos_f32_e32 v37, v37
	v_pk_mul_f32 v[180:181], v[110:111], v[34:35]
	v_pk_mul_f32 v[182:183], v[112:113], v[36:37]
	v_pk_fma_f32 v[180:181], v[114:115], v[30:31], v[180:181] neg_lo:[1,0,0] neg_hi:[1,0,0]
	v_pk_fma_f32 v[182:183], v[116:117], v[32:33], v[182:183] neg_lo:[1,0,0] neg_hi:[1,0,0]
	v_pk_mul_f32 v[114:115], v[114:115], v[34:35]
	v_pk_mul_f32 v[116:117], v[116:117], v[36:37]
	v_pk_fma_f32 v[114:115], v[110:111], v[30:31], v[114:115]
	v_pk_fma_f32 v[116:117], v[112:113], v[32:33], v[116:117]
	v_pk_mul_f32 v[110:111], v[180:181], v[12:13]
	v_pk_mul_f32 v[112:113], v[182:183], v[12:13]
	v_pk_mul_f32 v[114:115], v[114:115], v[12:13]
	v_pk_mul_f32 v[116:117], v[116:117], v[12:13]
	v_med3_f32 v110, v110, s35, v225
	v_med3_f32 v111, v111, s35, v225
	v_med3_f32 v112, v112, s35, v225
	v_med3_f32 v113, v113, s35, v225
	v_med3_f32 v114, v114, s35, v225
	v_med3_f32 v115, v115, s35, v225
	v_med3_f32 v116, v116, s35, v225
	v_med3_f32 v117, v117, s35, v225
	v_pk_mul_f32 v[34:35], v[18:19], v[24:25] op_sel:[0,1] op_sel_hi:[1,1]
	v_pk_mul_f32 v[36:37], v[20:21], v[24:25] op_sel:[0,1] op_sel_hi:[1,1]
	v_floor_f32_e32 v30, v34
	v_floor_f32_e32 v31, v35
	v_floor_f32_e32 v32, v36
	v_floor_f32_e32 v33, v37
	v_pk_fma_f32 v[34:35], v[18:19], v[24:25], v[30:31] op_sel:[0,1,0] op_sel_hi:[1,1,1] neg_lo:[0,0,1] neg_hi:[0,0,1]
; DI unsigned pk4_fp8(float a, float b, float c_, float d) { int w = 0; w = __builtin_amdgcn_cvt_pk_fp8_f32(clamp8(a), clamp8(b), w, false); w = __builtin_amdgcn_cvt_pk_fp8_f32(clamp8(c_), clamp8(d), w, true); return (unsigned)w; }
;     DI void operator()(const f32x4 (&acc)[2][2][4][2], const Unit& u, int wr, int wc, int fr, int fq) const {
;     ...
;             for (int ai = 0; ai < 2; ++ai) {
; #pragma unroll
;                 for (int m = 0; m < 4; ++m) {
;                     const int r = row0 + ai * 128 + m * 16; const float p = (float)posv[ai * 4 + m];
;                     unsigned char* rowp = (unsigned char*)base + dil_row(4 * tq + wc, r) + 8 * fq;
;                     u32x2 w1, w2;
; #pragma unroll
;                     for (int n = 0; n < 2; ++n) { f32x4 o1, o2;
; #pragma unroll
;                         for (int j = 0; j < 4; ++j) {
;                             float a = p * fre[n * 4 + j]; a = a - __builtin_floorf(a);
;                             const float sn = __builtin_amdgcn_sinf(a), cs = __builtin_amdgcn_cosf(a);
;                             const float x1 = acc[ai][0][m][n][j], x2 = acc[ai][1][m][n][j];
;                             o1[j] = (x1 * cs - x2 * sn) * sc; o2[j] = (x2 * cs + x1 * sn) * sc;
;                         }
;                         w1[n] = pk4_fp8(o1[0], o1[1], o1[2], o1[3]); w2[n] = pk4_fp8(o2[0], o2[1], o2[2], o2[3]); }
;                     st_pair16(rowp, 32, w1, w2, fq);
;                     asm volatile("" ::: "memory");
	v_pk_fma_f32 v[36:37], v[20:21], v[24:25], v[32:33] op_sel:[0,1,0] op_sel_hi:[1,1,1] neg_lo:[0,0,1] neg_hi:[0,0,1]
	v_sin_f32_e32 v30, v34
	v_sin_f32_e32 v31, v35
	v_sin_f32_e32 v32, v36
	v_sin_f32_e32 v33, v37
	v_cos_f32_e32 v34, v34
	v_cos_f32_e32 v35, v35
	v_cos_f32_e32 v36, v36
	v_cos_f32_e32 v37, v37
	v_pk_mul_f32 v[180:181], v[102:103], v[34:35]
	v_pk_mul_f32 v[182:183], v[104:105], v[36:37]
	v_pk_fma_f32 v[180:181], v[106:107], v[30:31], v[180:181] neg_lo:[1,0,0] neg_hi:[1,0,0]
	v_pk_fma_f32 v[182:183], v[108:109], v[32:33], v[182:183] neg_lo:[1,0,0] neg_hi:[1,0,0]
	v_pk_mul_f32 v[106:107], v[106:107], v[34:35]
	v_pk_mul_f32 v[108:109], v[108:109], v[36:37]
	v_pk_fma_f32 v[106:107], v[102:103], v[30:31], v[106:107]
	v_pk_fma_f32 v[108:109], v[104:105], v[32:33], v[108:109]
	v_pk_mul_f32 v[102:103], v[180:181], v[12:13]
	v_pk_mul_f32 v[104:105], v[182:183], v[12:13]
	v_pk_mul_f32 v[106:107], v[106:107], v[12:13]
	v_pk_mul_f32 v[108:109], v[108:109], v[12:13]
	v_med3_f32 v102, v102, s35, v225
	v_med3_f32 v103, v103, s35, v225
	v_med3_f32 v104, v104, s35, v225
	v_med3_f32 v105, v105, s35, v225
	v_med3_f32 v106, v106, s35, v225
	v_med3_f32 v107, v107, s35, v225
	v_med3_f32 v108, v108, s35, v225
	v_med3_f32 v109, v109, s35, v225
	v_cvt_pk_fp8_f32 v110, v110, v111
	v_cvt_pk_fp8_f32 v111, v102, v103
	v_cvt_pk_fp8_f32 v110, v112, v113 op_sel:[0,0,1]
	v_cvt_pk_fp8_f32 v111, v104, v105 op_sel:[0,0,1]
	v_cvt_pk_fp8_f32 v112, v114, v115
	v_cvt_pk_fp8_f32 v113, v106, v107
	v_cvt_pk_fp8_f32 v112, v116, v117 op_sel:[0,0,1]
	v_cvt_pk_fp8_f32 v113, v108, v109 op_sel:[0,0,1]
	s_nop 1
	v_permlane16_swap_b32_e32 v110, v112
	v_permlane16_swap_b32_e32 v111, v113
	global_store_dwordx4 v[8:9], v[110:113], off
	v_add_u32_e32 v11, 0x80, v10
	v_and_b32_e32 v9, 0xfff, v11
	v_lshrrev_b32_e32 v9, s4, v9
	v_and_b32_e32 v8, 0xfffff000, v11
	v_bitop3_b32 v11, v11, s30, v208 bitop3:0x20
	v_mad_u32_u24 v180, v11, s5, v9
	v_mov_b32_e32 v181, v4
	v_add_u32_e32 v8, s31, v8
	v_ashrrev_i32_e32 v9, 31, v8
	v_lshl_add_u64 v[8:9], v[180:181], 0, v[8:9]
	v_lshlrev_b64 v[8:9], 6, v[8:9]
	v_lshl_add_u64 v[8:9], v[6:7], 0, v[8:9]
	v_cvt_f32_i32_e32 v26, v26
	v_pk_mul_f32 v[34:35], v[14:15], v[26:27] op_sel_hi:[1,0]
	v_pk_mul_f32 v[36:37], v[16:17], v[26:27] op_sel_hi:[1,0]
	v_floor_f32_e32 v30, v34
	v_floor_f32_e32 v31, v35
	v_floor_f32_e32 v32, v36
	v_floor_f32_e32 v33, v37
	v_pk_fma_f32 v[34:35], v[14:15], v[26:27], v[30:31] op_sel_hi:[1,0,1] neg_lo:[0,0,1] neg_hi:[0,0,1]
	v_pk_fma_f32 v[36:37], v[16:17], v[26:27], v[32:33] op_sel_hi:[1,0,1] neg_lo:[0,0,1] neg_hi:[0,0,1]
	v_sin_f32_e32 v30, v34
	v_sin_f32_e32 v31, v35
	v_sin_f32_e32 v32, v36
	v_sin_f32_e32 v33, v37
	v_cos_f32_e32 v34, v34
	v_cos_f32_e32 v35, v35
	v_cos_f32_e32 v36, v36
	v_cos_f32_e32 v37, v37
	v_pk_mul_f32 v[180:181], v[94:95], v[34:35]
	v_pk_mul_f32 v[182:183], v[96:97], v[36:37]
	v_pk_fma_f32 v[180:181], v[98:99], v[30:31], v[180:181] neg_lo:[1,0,0] neg_hi:[1,0,0]
	v_pk_fma_f32 v[182:183], v[100:101], v[32:33], v[182:183] neg_lo:[1,0,0] neg_hi:[1,0,0]
	v_pk_mul_f32 v[98:99], v[98:99], v[34:35]
	v_pk_mul_f32 v[100:101], v[100:101], v[36:37]
	v_pk_fma_f32 v[98:99], v[94:95], v[30:31], v[98:99]
	v_pk_fma_f32 v[100:101], v[96:97], v[32:33], v[100:101]
	v_pk_mul_f32 v[94:95], v[180:181], v[12:13]
	v_pk_mul_f32 v[96:97], v[182:183], v[12:13]
	v_pk_mul_f32 v[98:99], v[98:99], v[12:13]
	v_pk_mul_f32 v[100:101], v[100:101], v[12:13]
	v_med3_f32 v94, v94, s35, v225
	v_med3_f32 v95, v95, s35, v225
	v_med3_f32 v96, v96, s35, v225
	v_med3_f32 v97, v97, s35, v225
	v_med3_f32 v98, v98, s35, v225
	v_med3_f32 v99, v99, s35, v225
	v_med3_f32 v100, v100, s35, v225
	v_med3_f32 v101, v101, s35, v225
	v_pk_mul_f32 v[34:35], v[18:19], v[26:27] op_sel_hi:[1,0]
	v_pk_mul_f32 v[36:37], v[20:21], v[26:27] op_sel_hi:[1,0]
	v_floor_f32_e32 v30, v34
	v_floor_f32_e32 v31, v35
	v_floor_f32_e32 v32, v36
	v_floor_f32_e32 v33, v37
	v_pk_fma_f32 v[34:35], v[18:19], v[26:27], v[30:31] op_sel_hi:[1,0,1] neg_lo:[0,0,1] neg_hi:[0,0,1]
	v_pk_fma_f32 v[36:37], v[20:21], v[26:27], v[32:33] op_sel_hi:[1,0,1] neg_lo:[0,0,1] neg_hi:[0,0,1]
	v_sin_f32_e32 v30, v34
	v_sin_f32_e32 v31, v35
	v_sin_f32_e32 v32, v36
	v_sin_f32_e32 v33, v37
	v_cos_f32_e32 v34, v34
	v_cos_f32_e32 v35, v35
	v_cos_f32_e32 v36, v36
	v_cos_f32_e32 v37, v37
	v_pk_mul_f32 v[180:181], v[86:87], v[34:35]
	v_pk_mul_f32 v[182:183], v[88:89], v[36:37]
	v_pk_fma_f32 v[180:181], v[90:91], v[30:31], v[180:181] neg_lo:[1,0,0] neg_hi:[1,0,0]
	v_pk_fma_f32 v[182:183], v[92:93], v[32:33], v[182:183] neg_lo:[1,0,0] neg_hi:[1,0,0]
	v_pk_mul_f32 v[90:91], v[90:91], v[34:35]
	v_pk_mul_f32 v[92:93], v[92:93], v[36:37]
	v_pk_fma_f32 v[90:91], v[86:87], v[30:31], v[90:91]
	v_pk_fma_f32 v[92:93], v[88:89], v[32:33], v[92:93]
	v_pk_mul_f32 v[86:87], v[180:181], v[12:13]
	v_pk_mul_f32 v[88:89], v[182:183], v[12:13]
	v_pk_mul_f32 v[90:91], v[90:91], v[12:13]
	v_pk_mul_f32 v[92:93], v[92:93], v[12:13]
	v_med3_f32 v86, v86, s35, v225
	v_med3_f32 v87, v87, s35, v225
	v_med3_f32 v88, v88, s35, v225
	v_med3_f32 v89, v89, s35, v225
	v_med3_f32 v90, v90, s35, v225
	v_med3_f32 v91, v91, s35, v225
	v_med3_f32 v92, v92, s35, v225
	v_med3_f32 v93, v93, s35, v225
	v_cvt_pk_fp8_f32 v94, v94, v95
	v_cvt_pk_fp8_f32 v95, v86, v87
	v_cvt_pk_fp8_f32 v94, v96, v97 op_sel:[0,0,1]
	v_cvt_pk_fp8_f32 v95, v88, v89 op_sel:[0,0,1]
	v_cvt_pk_fp8_f32 v96, v98, v99
	v_cvt_pk_fp8_f32 v97, v90, v91
	v_cvt_pk_fp8_f32 v96, v100, v101 op_sel:[0,0,1]
	v_cvt_pk_fp8_f32 v97, v92, v93 op_sel:[0,0,1]
	s_nop 1
	v_permlane16_swap_b32_e32 v94, v96
	v_permlane16_swap_b32_e32 v95, v97
	global_store_dwordx4 v[8:9], v[94:97], off
; DI unsigned pk4_fp8(float a, float b, float c_, float d) { int w = 0; w = __builtin_amdgcn_cvt_pk_fp8_f32(clamp8(a), clamp8(b), w, false); w = __builtin_amdgcn_cvt_pk_fp8_f32(clamp8(c_), clamp8(d), w, true); return (unsigned)w; }
;     DI void operator()(const f32x4 (&acc)[2][2][4][2], const Unit& u, int wr, int wc, int fr, int fq) const {
;     ...
;             for (int ai = 0; ai < 2; ++ai) {
; #pragma unroll
;                 for (int m = 0; m < 4; ++m) {
;                     const int r = row0 + ai * 128 + m * 16; const float p = (float)posv[ai * 4 + m];
;                     unsigned char* rowp = (unsigned char*)base + dil_row(4 * tq + wc, r) + 8 * fq;
;                     u32x2 w1, w2;
; #pragma unroll
;                     for (int n = 0; n < 2; ++n) { f32x4 o1, o2;
; #pragma unroll
;                         for (int j = 0; j < 4; ++j) {
;                             float a = p * fre[n * 4 + j]; a = a - __builtin_floorf(a);
;                             const float sn = __builtin_amdgcn_sinf(a), cs = __builtin_amdgcn_cosf(a);
;                             const float x1 = acc[ai][0][m][n][j], x2 = acc[ai][1][m][n][j];
;                             o1[j] = (x1 * cs - x2 * sn) * sc; o2[j] = (x2 * cs + x1 * sn) * sc;
;                         }
;                         w1[n] = pk4_fp8(o1[0], o1[1], o1[2], o1[3]); w2[n] = pk4_fp8(o2[0], o2[1], o2[2], o2[3]); }
;                     st_pair16(rowp, 32, w1, w2, fq);
;                     asm volatile("" ::: "memory");
	v_add_u32_e32 v11, 0x90, v10
	v_and_b32_e32 v9, 0xfff, v11
	v_lshrrev_b32_e32 v9, s4, v9
	v_and_b32_e32 v8, 0xfffff000, v11
	v_bitop3_b32 v11, v11, s30, v208 bitop3:0x20
	v_mad_u32_u24 v180, v11, s5, v9
	v_mov_b32_e32 v181, v4
	v_add_u32_e32 v8, s31, v8
	v_ashrrev_i32_e32 v9, 31, v8
	v_lshl_add_u64 v[8:9], v[180:181], 0, v[8:9]
	v_lshlrev_b64 v[8:9], 6, v[8:9]
	v_lshl_add_u64 v[8:9], v[6:7], 0, v[8:9]
	v_cvt_f32_i32_e32 v27, v27
	v_pk_mul_f32 v[34:35], v[14:15], v[26:27] op_sel:[0,1] op_sel_hi:[1,1]
	v_pk_mul_f32 v[36:37], v[16:17], v[26:27] op_sel:[0,1] op_sel_hi:[1,1]
	v_floor_f32_e32 v30, v34
	v_floor_f32_e32 v31, v35
	v_floor_f32_e32 v32, v36
	v_floor_f32_e32 v33, v37
	v_pk_fma_f32 v[34:35], v[14:15], v[26:27], v[30:31] op_sel:[0,1,0] op_sel_hi:[1,1,1] neg_lo:[0,0,1] neg_hi:[0,0,1]
	v_pk_fma_f32 v[36:37], v[16:17], v[26:27], v[32:33] op_sel:[0,1,0] op_sel_hi:[1,1,1] neg_lo:[0,0,1] neg_hi:[0,0,1]
	v_sin_f32_e32 v30, v34
	v_sin_f32_e32 v31, v35
	v_sin_f32_e32 v32, v36
	v_sin_f32_e32 v33, v37
	v_cos_f32_e32 v34, v34
	v_cos_f32_e32 v35, v35
	v_cos_f32_e32 v36, v36
	v_cos_f32_e32 v37, v37
	v_pk_mul_f32 v[180:181], v[78:79], v[34:35]
	v_pk_mul_f32 v[182:183], v[80:81], v[36:37]
	v_pk_fma_f32 v[180:181], v[82:83], v[30:31], v[180:181] neg_lo:[1,0,0] neg_hi:[1,0,0]
	v_pk_fma_f32 v[182:183], v[84:85], v[32:33], v[182:183] neg_lo:[1,0,0] neg_hi:[1,0,0]
	v_pk_mul_f32 v[82:83], v[82:83], v[34:35]
	v_pk_mul_f32 v[84:85], v[84:85], v[36:37]
	v_pk_fma_f32 v[82:83], v[78:79], v[30:31], v[82:83]
	v_pk_fma_f32 v[84:85], v[80:81], v[32:33], v[84:85]
	v_pk_mul_f32 v[78:79], v[180:181], v[12:13]
	v_pk_mul_f32 v[80:81], v[182:183], v[12:13]
	v_pk_mul_f32 v[82:83], v[82:83], v[12:13]
	v_pk_mul_f32 v[84:85], v[84:85], v[12:13]
	v_med3_f32 v78, v78, s35, v225
	v_med3_f32 v79, v79, s35, v225
	v_med3_f32 v80, v80, s35, v225
	v_med3_f32 v81, v81, s35, v225
	v_med3_f32 v82, v82, s35, v225
	v_med3_f32 v83, v83, s35, v225
	v_med3_f32 v84, v84, s35, v225
	v_med3_f32 v85, v85, s35, v225
	v_pk_mul_f32 v[34:35], v[18:19], v[26:27] op_sel:[0,1] op_sel_hi:[1,1]
	v_pk_mul_f32 v[36:37], v[20:21], v[26:27] op_sel:[0,1] op_sel_hi:[1,1]
	v_floor_f32_e32 v30, v34
	v_floor_f32_e32 v31, v35
	v_floor_f32_e32 v32, v36
	v_floor_f32_e32 v33, v37
	v_pk_fma_f32 v[34:35], v[18:19], v[26:27], v[30:31] op_sel:[0,1,0] op_sel_hi:[1,1,1] neg_lo:[0,0,1] neg_hi:[0,0,1]
	v_pk_fma_f32 v[36:37], v[20:21], v[26:27], v[32:33] op_sel:[0,1,0] op_sel_hi:[1,1,1] neg_lo:[0,0,1] neg_hi:[0,0,1]
	v_sin_f32_e32 v30, v34
	v_sin_f32_e32 v31, v35
	v_sin_f32_e32 v32, v36
	v_sin_f32_e32 v33, v37
	v_cos_f32_e32 v34, v34
	v_cos_f32_e32 v35, v35
	v_cos_f32_e32 v36, v36
	v_cos_f32_e32 v37, v37
	v_pk_mul_f32 v[180:181], v[70:71], v[34:35]
	v_pk_mul_f32 v[182:183], v[72:73], v[36:37]
	v_pk_fma_f32 v[180:181], v[74:75], v[30:31], v[180:181] neg_lo:[1,0,0] neg_hi:[1,0,0]
	v_pk_fma_f32 v[182:183], v[76:77], v[32:33], v[182:183] neg_lo:[1,0,0] neg_hi:[1,0,0]
	v_pk_mul_f32 v[74:75], v[74:75], v[34:35]
	v_pk_mul_f32 v[76:77], v[76:77], v[36:37]
	v_pk_fma_f32 v[74:75], v[70:71], v[30:31], v[74:75]
	v_pk_fma_f32 v[76:77], v[72:73], v[32:33], v[76:77]
	v_pk_mul_f32 v[70:71], v[180:181], v[12:13]
	v_pk_mul_f32 v[72:73], v[182:183], v[12:13]
	v_pk_mul_f32 v[74:75], v[74:75], v[12:13]
	v_pk_mul_f32 v[76:77], v[76:77], v[12:13]
	v_med3_f32 v70, v70, s35, v225
	v_med3_f32 v71, v71, s35, v225
	v_med3_f32 v72, v72, s35, v225
	v_med3_f32 v73, v73, s35, v225
	v_med3_f32 v74, v74, s35, v225
	v_med3_f32 v75, v75, s35, v225
	v_med3_f32 v76, v76, s35, v225
	v_med3_f32 v77, v77, s35, v225
	v_cvt_pk_fp8_f32 v78, v78, v79
	v_cvt_pk_fp8_f32 v79, v70, v71
	v_cvt_pk_fp8_f32 v78, v80, v81 op_sel:[0,0,1]
	v_cvt_pk_fp8_f32 v79, v72, v73 op_sel:[0,0,1]
	v_cvt_pk_fp8_f32 v80, v82, v83
	v_cvt_pk_fp8_f32 v81, v74, v75
	v_cvt_pk_fp8_f32 v80, v84, v85 op_sel:[0,0,1]
	v_cvt_pk_fp8_f32 v81, v76, v77 op_sel:[0,0,1]
	s_nop 1
	v_permlane16_swap_b32_e32 v78, v80
	v_permlane16_swap_b32_e32 v79, v81
	global_store_dwordx4 v[8:9], v[78:81], off
	v_add_u32_e32 v11, 0xa0, v10
	v_and_b32_e32 v9, 0xfff, v11
	v_lshrrev_b32_e32 v9, s4, v9
	v_and_b32_e32 v8, 0xfffff000, v11
	v_bitop3_b32 v11, v11, s30, v208 bitop3:0x20
	v_mad_u32_u24 v180, v11, s5, v9
	v_mov_b32_e32 v181, v4
	v_add_u32_e32 v8, s31, v8
	v_ashrrev_i32_e32 v9, 31, v8
	v_lshl_add_u64 v[8:9], v[180:181], 0, v[8:9]
	v_lshlrev_b64 v[8:9], 6, v[8:9]
	v_lshl_add_u64 v[8:9], v[6:7], 0, v[8:9]
	v_cvt_f32_i32_e32 v28, v28
	v_pk_mul_f32 v[34:35], v[14:15], v[28:29] op_sel_hi:[1,0]
	v_pk_mul_f32 v[36:37], v[16:17], v[28:29] op_sel_hi:[1,0]
	v_floor_f32_e32 v30, v34
	v_floor_f32_e32 v31, v35
	v_floor_f32_e32 v32, v36
	v_floor_f32_e32 v33, v37
	v_pk_fma_f32 v[34:35], v[14:15], v[28:29], v[30:31] op_sel_hi:[1,0,1] neg_lo:[0,0,1] neg_hi:[0,0,1]
	v_pk_fma_f32 v[36:37], v[16:17], v[28:29], v[32:33] op_sel_hi:[1,0,1] neg_lo:[0,0,1] neg_hi:[0,0,1]
	v_sin_f32_e32 v30, v34
	v_sin_f32_e32 v31, v35
	v_sin_f32_e32 v32, v36
	v_sin_f32_e32 v33, v37
	v_cos_f32_e32 v34, v34
	v_cos_f32_e32 v35, v35
	v_cos_f32_e32 v36, v36
	v_cos_f32_e32 v37, v37
	v_pk_mul_f32 v[180:181], v[62:63], v[34:35]
	v_pk_mul_f32 v[182:183], v[64:65], v[36:37]
	v_pk_fma_f32 v[180:181], v[66:67], v[30:31], v[180:181] neg_lo:[1,0,0] neg_hi:[1,0,0]
	v_pk_fma_f32 v[182:183], v[68:69], v[32:33], v[182:183] neg_lo:[1,0,0] neg_hi:[1,0,0]
	v_pk_mul_f32 v[66:67], v[66:67], v[34:35]
	v_pk_mul_f32 v[68:69], v[68:69], v[36:37]
	v_pk_fma_f32 v[66:67], v[62:63], v[30:31], v[66:67]
	v_pk_fma_f32 v[68:69], v[64:65], v[32:33], v[68:69]
	v_pk_mul_f32 v[62:63], v[180:181], v[12:13]
	v_pk_mul_f32 v[64:65], v[182:183], v[12:13]
	v_pk_mul_f32 v[66:67], v[66:67], v[12:13]
; DI unsigned pk4_fp8(float a, float b, float c_, float d) { int w = 0; w = __builtin_amdgcn_cvt_pk_fp8_f32(clamp8(a), clamp8(b), w, false); w = __builtin_amdgcn_cvt_pk_fp8_f32(clamp8(c_), clamp8(d), w, true); return (unsigned)w; }
;     DI void operator()(const f32x4 (&acc)[2][2][4][2], const Unit& u, int wr, int wc, int fr, int fq) const {
;     ...
;             for (int ai = 0; ai < 2; ++ai) {
; #pragma unroll
;                 for (int m = 0; m < 4; ++m) {
;                     const int r = row0 + ai * 128 + m * 16; const float p = (float)posv[ai * 4 + m];
;                     unsigned char* rowp = (unsigned char*)base + dil_row(4 * tq + wc, r) + 8 * fq;
;                     u32x2 w1, w2;
; #pragma unroll
;                     for (int n = 0; n < 2; ++n) { f32x4 o1, o2;
; #pragma unroll
;                         for (int j = 0; j < 4; ++j) {
;                             float a = p * fre[n * 4 + j]; a = a - __builtin_floorf(a);
;                             const float sn = __builtin_amdgcn_sinf(a), cs = __builtin_amdgcn_cosf(a);
;                             const float x1 = acc[ai][0][m][n][j], x2 = acc[ai][1][m][n][j];
;                             o1[j] = (x1 * cs - x2 * sn) * sc; o2[j] = (x2 * cs + x1 * sn) * sc;
;                         }
;                         w1[n] = pk4_fp8(o1[0], o1[1], o1[2], o1[3]); w2[n] = pk4_fp8(o2[0], o2[1], o2[2], o2[3]); }
;                     st_pair16(rowp, 32, w1, w2, fq);
;                     asm volatile("" ::: "memory");
	v_pk_mul_f32 v[68:69], v[68:69], v[12:13]
	v_med3_f32 v62, v62, s35, v225
	v_med3_f32 v63, v63, s35, v225
	v_med3_f32 v64, v64, s35, v225
	v_med3_f32 v65, v65, s35, v225
	v_med3_f32 v66, v66, s35, v225
	v_med3_f32 v67, v67, s35, v225
	v_med3_f32 v68, v68, s35, v225
	v_med3_f32 v69, v69, s35, v225
	v_pk_mul_f32 v[34:35], v[18:19], v[28:29] op_sel_hi:[1,0]
	v_pk_mul_f32 v[36:37], v[20:21], v[28:29] op_sel_hi:[1,0]
	v_floor_f32_e32 v30, v34
	v_floor_f32_e32 v31, v35
	v_floor_f32_e32 v32, v36
	v_floor_f32_e32 v33, v37
	v_pk_fma_f32 v[34:35], v[18:19], v[28:29], v[30:31] op_sel_hi:[1,0,1] neg_lo:[0,0,1] neg_hi:[0,0,1]
	v_pk_fma_f32 v[36:37], v[20:21], v[28:29], v[32:33] op_sel_hi:[1,0,1] neg_lo:[0,0,1] neg_hi:[0,0,1]
	v_sin_f32_e32 v30, v34
	v_sin_f32_e32 v31, v35
	v_sin_f32_e32 v32, v36
	v_sin_f32_e32 v33, v37
	v_cos_f32_e32 v34, v34
	v_cos_f32_e32 v35, v35
	v_cos_f32_e32 v36, v36
	v_cos_f32_e32 v37, v37
	v_pk_mul_f32 v[180:181], v[54:55], v[34:35]
	v_pk_mul_f32 v[182:183], v[56:57], v[36:37]
	v_pk_fma_f32 v[180:181], v[58:59], v[30:31], v[180:181] neg_lo:[1,0,0] neg_hi:[1,0,0]
	v_pk_fma_f32 v[182:183], v[60:61], v[32:33], v[182:183] neg_lo:[1,0,0] neg_hi:[1,0,0]
	v_pk_mul_f32 v[58:59], v[58:59], v[34:35]
	v_pk_mul_f32 v[60:61], v[60:61], v[36:37]
	v_pk_fma_f32 v[58:59], v[54:55], v[30:31], v[58:59]
	v_pk_fma_f32 v[60:61], v[56:57], v[32:33], v[60:61]
	v_pk_mul_f32 v[54:55], v[180:181], v[12:13]
	v_pk_mul_f32 v[56:57], v[182:183], v[12:13]
	v_pk_mul_f32 v[58:59], v[58:59], v[12:13]
	v_pk_mul_f32 v[60:61], v[60:61], v[12:13]
	v_med3_f32 v54, v54, s35, v225
	v_med3_f32 v55, v55, s35, v225
	v_med3_f32 v56, v56, s35, v225
	v_med3_f32 v57, v57, s35, v225
	v_med3_f32 v58, v58, s35, v225
	v_med3_f32 v59, v59, s35, v225
	v_med3_f32 v60, v60, s35, v225
	v_med3_f32 v61, v61, s35, v225
	v_cvt_pk_fp8_f32 v62, v62, v63
	v_cvt_pk_fp8_f32 v63, v54, v55
	v_cvt_pk_fp8_f32 v62, v64, v65 op_sel:[0,0,1]
	v_cvt_pk_fp8_f32 v63, v56, v57 op_sel:[0,0,1]
	v_cvt_pk_fp8_f32 v64, v66, v67
	v_cvt_pk_fp8_f32 v65, v58, v59
	v_cvt_pk_fp8_f32 v64, v68, v69 op_sel:[0,0,1]
	v_cvt_pk_fp8_f32 v65, v60, v61 op_sel:[0,0,1]
	s_nop 1
	v_permlane16_swap_b32_e32 v62, v64
	v_permlane16_swap_b32_e32 v63, v65
	global_store_dwordx4 v[8:9], v[62:65], off
	v_add_u32_e32 v11, 0xb0, v10
	v_and_b32_e32 v9, 0xfff, v11
	v_lshrrev_b32_e32 v9, s4, v9
	v_and_b32_e32 v8, 0xfffff000, v11
	v_bitop3_b32 v11, v11, s30, v208 bitop3:0x20
	v_mad_u32_u24 v180, v11, s5, v9
	v_mov_b32_e32 v181, v4
	v_add_u32_e32 v8, s31, v8
	v_ashrrev_i32_e32 v9, 31, v8
	v_lshl_add_u64 v[8:9], v[180:181], 0, v[8:9]
	v_lshlrev_b64 v[8:9], 6, v[8:9]
	v_lshl_add_u64 v[8:9], v[6:7], 0, v[8:9]
	v_cvt_f32_i32_e32 v29, v29
	v_pk_mul_f32 v[34:35], v[14:15], v[28:29] op_sel:[0,1] op_sel_hi:[1,1]
	v_pk_mul_f32 v[36:37], v[16:17], v[28:29] op_sel:[0,1] op_sel_hi:[1,1]
	v_floor_f32_e32 v30, v34
	v_floor_f32_e32 v31, v35
	v_floor_f32_e32 v32, v36
	v_floor_f32_e32 v33, v37
	v_pk_fma_f32 v[34:35], v[14:15], v[28:29], v[30:31] op_sel:[0,1,0] op_sel_hi:[1,1,1] neg_lo:[0,0,1] neg_hi:[0,0,1]
	v_pk_fma_f32 v[36:37], v[16:17], v[28:29], v[32:33] op_sel:[0,1,0] op_sel_hi:[1,1,1] neg_lo:[0,0,1] neg_hi:[0,0,1]
	v_sin_f32_e32 v30, v34
	v_sin_f32_e32 v31, v35
	v_sin_f32_e32 v32, v36
	v_sin_f32_e32 v33, v37
	v_cos_f32_e32 v34, v34
	v_cos_f32_e32 v35, v35
	v_cos_f32_e32 v36, v36
	v_cos_f32_e32 v37, v37
	v_pk_mul_f32 v[180:181], v[46:47], v[34:35]
	v_pk_mul_f32 v[182:183], v[48:49], v[36:37]
	v_pk_fma_f32 v[180:181], v[50:51], v[30:31], v[180:181] neg_lo:[1,0,0] neg_hi:[1,0,0]
	v_pk_fma_f32 v[182:183], v[52:53], v[32:33], v[182:183] neg_lo:[1,0,0] neg_hi:[1,0,0]
	v_pk_mul_f32 v[50:51], v[50:51], v[34:35]
	v_pk_mul_f32 v[52:53], v[52:53], v[36:37]
	v_pk_fma_f32 v[50:51], v[46:47], v[30:31], v[50:51]
	v_pk_fma_f32 v[52:53], v[48:49], v[32:33], v[52:53]
	v_pk_mul_f32 v[46:47], v[180:181], v[12:13]
	v_pk_mul_f32 v[48:49], v[182:183], v[12:13]
	v_pk_mul_f32 v[50:51], v[50:51], v[12:13]
	v_pk_mul_f32 v[52:53], v[52:53], v[12:13]
	v_med3_f32 v46, v46, s35, v225
	v_med3_f32 v47, v47, s35, v225
	v_med3_f32 v48, v48, s35, v225
	v_med3_f32 v49, v49, s35, v225
	v_med3_f32 v50, v50, s35, v225
	v_med3_f32 v51, v51, s35, v225
	v_med3_f32 v52, v52, s35, v225
	v_med3_f32 v53, v53, s35, v225
	v_pk_mul_f32 v[34:35], v[18:19], v[28:29] op_sel:[0,1] op_sel_hi:[1,1]
	v_pk_mul_f32 v[36:37], v[20:21], v[28:29] op_sel:[0,1] op_sel_hi:[1,1]
	v_floor_f32_e32 v30, v34
	v_floor_f32_e32 v31, v35
	v_floor_f32_e32 v32, v36
	v_floor_f32_e32 v33, v37
	v_pk_fma_f32 v[34:35], v[18:19], v[28:29], v[30:31] op_sel:[0,1,0] op_sel_hi:[1,1,1] neg_lo:[0,0,1] neg_hi:[0,0,1]
	v_pk_fma_f32 v[36:37], v[20:21], v[28:29], v[32:33] op_sel:[0,1,0] op_sel_hi:[1,1,1] neg_lo:[0,0,1] neg_hi:[0,0,1]
	v_sin_f32_e32 v30, v34
	v_sin_f32_e32 v31, v35
	v_sin_f32_e32 v32, v36
	v_sin_f32_e32 v33, v37
	v_cos_f32_e32 v34, v34
	v_cos_f32_e32 v35, v35
	v_cos_f32_e32 v36, v36
	v_cos_f32_e32 v37, v37
	v_pk_mul_f32 v[180:181], v[38:39], v[34:35]
	v_pk_mul_f32 v[182:183], v[40:41], v[36:37]
	v_pk_fma_f32 v[180:181], v[42:43], v[30:31], v[180:181] neg_lo:[1,0,0] neg_hi:[1,0,0]
	v_pk_fma_f32 v[182:183], v[44:45], v[32:33], v[182:183] neg_lo:[1,0,0] neg_hi:[1,0,0]
	v_pk_mul_f32 v[42:43], v[42:43], v[34:35]
	v_pk_mul_f32 v[44:45], v[44:45], v[36:37]
	v_pk_fma_f32 v[42:43], v[38:39], v[30:31], v[42:43]
	v_pk_fma_f32 v[44:45], v[40:41], v[32:33], v[44:45]
	v_pk_mul_f32 v[38:39], v[180:181], v[12:13]
	v_pk_mul_f32 v[40:41], v[182:183], v[12:13]
	v_pk_mul_f32 v[42:43], v[42:43], v[12:13]
	v_pk_mul_f32 v[44:45], v[44:45], v[12:13]
	v_med3_f32 v38, v38, s35, v225
	v_med3_f32 v39, v39, s35, v225
	v_med3_f32 v40, v40, s35, v225
	v_med3_f32 v41, v41, s35, v225
	v_med3_f32 v42, v42, s35, v225
	v_med3_f32 v43, v43, s35, v225
	v_med3_f32 v44, v44, s35, v225
	v_med3_f32 v45, v45, s35, v225
	v_cvt_pk_fp8_f32 v46, v46, v47
	v_cvt_pk_fp8_f32 v47, v38, v39
	v_cvt_pk_fp8_f32 v46, v48, v49 op_sel:[0,0,1]
	v_cvt_pk_fp8_f32 v47, v40, v41 op_sel:[0,0,1]
	v_cvt_pk_fp8_f32 v48, v50, v51
	v_cvt_pk_fp8_f32 v49, v42, v43
	v_cvt_pk_fp8_f32 v48, v52, v53 op_sel:[0,0,1]
	v_cvt_pk_fp8_f32 v49, v44, v45 op_sel:[0,0,1]
	s_nop 1
	v_permlane16_swap_b32_e32 v46, v48
	v_permlane16_swap_b32_e32 v47, v49
	global_store_dwordx4 v[8:9], v[46:49], off
	s_andn2_b64 vcc, exec, s[40:41]
	s_mov_b64 s[16:17], -1
	s_cbranch_vccnz .LBB0_272
	s_branch .LBB0_316
